# up-GEMM: per-unit expert-count load issued in the unit preheader instead of inside the K-loop (removes a vmcnt(0) DMA drain per unit)
# speedup vs baseline: 1.0061x; 1.0022x over previous
; #define LAS __attribute__((address_space(3)))
; __device__ __forceinline__ int lane_id() { int l; asm volatile("v_mbcnt_lo_u32_b32 %0, -1, 0\n\tv_mbcnt_hi_u32_b32 %0, -1, %0" : "=v"(l)); return l; }
;     __device__ __forceinline__ bool next(int i, Unit& u) const { if (!SchedMoE::next_tab(i, u)) return false; u.a0 = A + (size_t)u.p0 * 256 * rowbytes; u.a1 = u.a0 + (size_t)128 * rowbytes; return true; }
;     ...
;     for (;;) {
;         const bool has_next = S.next(ui + 1, nxt);
;         if (!has_next) nxt = cur;
;         nxt.q = (ui + 1) & 1;
;         for (int t = 0; t < nt; t += 2) {
;             const bool last = (t == nt - 2);
;             { const int tz_ = wid * 64 + lane_id();
; #pragma unroll
;               for (int i = 0; i < 2; ++i) { int R, C; stage_rc(tz_ * 16 + i * 8192, R, C); const int Rb = Epi::PERM ? ((R & ~31) + perm32(R & 31)) : R;
;                   voffA[i] = (unsigned)(R * S.multA * S.pitchA + C) * 2u; voffB[i] = (unsigned)(Rb * S.multB * S.pitchB + C) * 2u; } }
;     __device__ __forceinline__ void prefetch(const Unit& u, LAS unsigned char* lds) const {
;         LAS unsigned char* blk = lds + LDS_STAGE + u.q * 4096;
;         const int wid = wv, e = u.p2; int lane = lane_id(); asm volatile("" : "+v"(lane));
;         const int n = (int)cnt[64 * e]; int pos = u.p3 + (wid & 3) * 64 + lane; pos = pos < n ? pos : n - 1;
.LBB0_1624:
	s_andn2_b64 vcc, exec, s[8:9]
	s_and_b32 s20, s43, 1
	s_cbranch_vccnz .LBB0_1638
	s_lshl_b32 s21, s20, 12
	s_lshl_b32 s26, s48, 6
	s_add_i32 s21, s21, 0
	s_ashr_i32 s27, s26, 31
	s_ashr_i32 s49, s48, 31
	s_lshl_b32 s70, s1, 7
	s_lshl_b32 s80, s1, 8
	s_add_i32 s21, s21, 0x20000
	s_lshl_b64 s[36:37], s[48:49], 16
	s_lshl_b64 s[72:73], s[48:49], 14
	s_ashr_i32 s71, s70, 31
	s_ashr_i32 s81, s80, 31
	s_lshl_b64 s[26:27], s[26:27], 2
	v_readlane_b32 s31, v255, 18
	s_add_u32 s64, s31, s26
	s_addc_u32 s65, s47, s27
	s_add_i32 s49, s24, s10
	s_add_u32 s66, s84, s36
	s_addc_u32 s67, s86, s37
	v_readlane_b32 s26, v255, 14
	s_add_u32 s68, s26, s36
	v_readlane_b32 s26, v255, 16
	s_addc_u32 s69, s26, s37
	s_add_u32 s31, s12, s72
	s_addc_u32 s36, s13, s73
	s_lshl_b64 s[26:27], s[70:71], 2
	s_add_u32 s70, s31, s26
	s_addc_u32 s71, s36, s27
	v_readlane_b32 s26, v255, 19
	s_add_u32 s31, s26, s72
	v_readlane_b32 s26, v255, 22
	s_addc_u32 s36, s26, s73
	s_lshl_b64 s[26:27], s[80:81], 2
	s_add_u32 s72, s31, s26
	s_addc_u32 s73, s36, s27
	s_add_u32 s36, s74, 0x100
	s_addc_u32 s37, s75, 0
	s_add_u32 s87, s76, 0x100
	s_addc_u32 s90, s77, 0
	s_add_u32 s26, s78, 0x100
	s_addc_u32 s27, s79, 0
	s_mov_b32 s31, 0
	s_mov_b64 s[74:75], 0
	v_mov_b32_e32 v0, 0
	v_mov_b32_e32 v1, 0
	v_mov_b32_e32 v2, 0
	v_mov_b32_e32 v3, 0
	v_mov_b32_e32 v8, 0
	v_mov_b32_e32 v9, 0
	v_mov_b32_e32 v10, 0
	v_mov_b32_e32 v11, 0
	v_mov_b32_e32 v16, 0
	v_mov_b32_e32 v17, 0
	v_mov_b32_e32 v18, 0
	v_mov_b32_e32 v19, 0
	v_mov_b32_e32 v24, 0
	v_mov_b32_e32 v25, 0
	v_mov_b32_e32 v26, 0
	v_mov_b32_e32 v27, 0
	v_mov_b32_e32 v32, 0
	v_mov_b32_e32 v33, 0
	v_mov_b32_e32 v34, 0
	v_mov_b32_e32 v35, 0
	v_mov_b32_e32 v40, 0
	v_mov_b32_e32 v41, 0
	v_mov_b32_e32 v42, 0
	v_mov_b32_e32 v43, 0
	v_mov_b32_e32 v48, 0
	v_mov_b32_e32 v49, 0
	v_mov_b32_e32 v50, 0
	v_mov_b32_e32 v51, 0
	v_mov_b32_e32 v56, 0
	v_mov_b32_e32 v57, 0
	v_mov_b32_e32 v58, 0
	v_mov_b32_e32 v59, 0
	v_mov_b32_e32 v4, 0
	v_mov_b32_e32 v5, 0
	v_mov_b32_e32 v6, 0
	v_mov_b32_e32 v7, 0
	v_mov_b32_e32 v12, 0
	v_mov_b32_e32 v13, 0
	v_mov_b32_e32 v14, 0
	v_mov_b32_e32 v15, 0
	v_mov_b32_e32 v20, 0
	v_mov_b32_e32 v21, 0
	v_mov_b32_e32 v22, 0
	v_mov_b32_e32 v23, 0
	v_mov_b32_e32 v28, 0
	v_mov_b32_e32 v29, 0
	v_mov_b32_e32 v30, 0
	v_mov_b32_e32 v31, 0
	v_mov_b32_e32 v36, 0
	v_mov_b32_e32 v37, 0
	v_mov_b32_e32 v38, 0
	v_mov_b32_e32 v39, 0
	v_mov_b32_e32 v44, 0
	v_mov_b32_e32 v45, 0
	v_mov_b32_e32 v46, 0
	v_mov_b32_e32 v47, 0
	v_mov_b32_e32 v52, 0
	v_mov_b32_e32 v53, 0
	v_mov_b32_e32 v54, 0
	v_mov_b32_e32 v55, 0
	v_mov_b32_e32 v60, 0
	v_mov_b32_e32 v61, 0
	v_mov_b32_e32 v62, 0
	v_mov_b32_e32 v63, 0
	v_mov_b32_e32 v80, 0
	v_mov_b32_e32 v81, 0
	v_mov_b32_e32 v82, 0
	v_mov_b32_e32 v83, 0
	v_mov_b32_e32 v104, 0
	v_mov_b32_e32 v105, 0
	v_mov_b32_e32 v106, 0
	v_mov_b32_e32 v107, 0
	v_mov_b32_e32 v112, 0
	v_mov_b32_e32 v113, 0
	v_mov_b32_e32 v114, 0
	v_mov_b32_e32 v115, 0
	v_mov_b32_e32 v120, 0
	v_mov_b32_e32 v121, 0
	v_mov_b32_e32 v122, 0
	v_mov_b32_e32 v123, 0
	v_mov_b32_e32 v128, 0
	v_mov_b32_e32 v129, 0
	v_mov_b32_e32 v130, 0
	v_mov_b32_e32 v131, 0
	v_mov_b32_e32 v136, 0
	v_mov_b32_e32 v137, 0
	v_mov_b32_e32 v138, 0
	v_mov_b32_e32 v139, 0
	v_mov_b32_e32 v144, 0
	v_mov_b32_e32 v145, 0
	v_mov_b32_e32 v146, 0
	v_mov_b32_e32 v147, 0
	v_mov_b32_e32 v152, 0
	v_mov_b32_e32 v153, 0
	v_mov_b32_e32 v154, 0
	v_mov_b32_e32 v155, 0
	v_mov_b32_e32 v84, 0
	v_mov_b32_e32 v85, 0
	v_mov_b32_e32 v86, 0
	v_mov_b32_e32 v87, 0
	v_mov_b32_e32 v108, 0
	v_mov_b32_e32 v109, 0
	v_mov_b32_e32 v110, 0
	v_mov_b32_e32 v111, 0
	v_mov_b32_e32 v116, 0
	v_mov_b32_e32 v117, 0
	v_mov_b32_e32 v118, 0
	v_mov_b32_e32 v119, 0
	v_mov_b32_e32 v124, 0
	v_mov_b32_e32 v125, 0
	v_mov_b32_e32 v126, 0
	v_mov_b32_e32 v127, 0
	v_mov_b32_e32 v132, 0
	v_mov_b32_e32 v133, 0
	v_mov_b32_e32 v134, 0
	v_mov_b32_e32 v135, 0
	v_mov_b32_e32 v140, 0
	v_mov_b32_e32 v141, 0
	v_mov_b32_e32 v142, 0
	v_mov_b32_e32 v143, 0
	v_mov_b32_e32 v148, 0
	v_mov_b32_e32 v149, 0
	v_mov_b32_e32 v150, 0
	v_mov_b32_e32 v151, 0
	v_mov_b32_e32 v156, 0
	v_mov_b32_e32 v157, 0
	v_mov_b32_e32 v158, 0
	v_mov_b32_e32 v159, 0
	v_mbcnt_lo_u32_b32 v248, -1, 0
	v_mbcnt_hi_u32_b32 v248, -1, v248
	v_mov_b32_e32 v249, s88
	v_lshrrev_b32_e32 v249, 6, v249
	v_and_b32_e32 v250, 3, v248
	v_lshlrev_b32_e32 v250, 4, v250
	v_and_b32_e32 v251, 32, v248
	v_xor_b32_e32 v250, v250, v251
	v_and_b32_e32 v251, 1, v249
	v_lshl_add_u32 v250, v251, 6, v250
	v_lshrrev_b32_e32 v251, 1, v249
	v_lshrrev_b32_e32 v252, 2, v248
	v_lshl_add_u32 v251, v251, 4, v252
	v_lshrrev_b32_e32 v251, 2, v249
	v_lshlrev_b32_e32 v251, 5, v251
	v_lshrrev_b32_e32 v252, 4, v248
	v_lshl_add_u32 v251, v252, 3, v251
	v_bfe_u32 v252, v249, 1, 1
	v_lshl_add_u32 v251, v252, 2, v251
	v_bfe_u32 v252, v248, 2, 2
	v_add_u32_e32 v251, v251, v252
	v_mov_b32_e32 v253, 0x800
	v_mad_u32_u24 v244, v251, v253, v250
	v_add_u32_e32 v246, 0x20000, v244
	v_mov_b32_e32 v245, 0
	v_mov_b32_e32 v247, 0
	global_load_dword v230, v245, s[64:65]
	s_branch .LBB0_1627

; #define LAS __attribute__((address_space(3)))
; __device__ __forceinline__ int lane_id() { int l; asm volatile("v_mbcnt_lo_u32_b32 %0, -1, 0\n\tv_mbcnt_hi_u32_b32 %0, -1, %0" : "=v"(l)); return l; }
;     __device__ __forceinline__ void prefetch(const Unit& u, LAS unsigned char* lds) const {
;         LAS unsigned char* blk = lds + LDS_STAGE + u.q * 4096;
;         const int wid = wv, e = u.p2; int lane = lane_id(); asm volatile("" : "+v"(lane));
;         const int n = (int)cnt[64 * e]; int pos = u.p3 + (wid & 3) * 64 + lane; pos = pos < n ? pos : n - 1;
;         if (wid < 4) __builtin_amdgcn_global_load_lds((const unsigned*)(row_tok + (size_t)e * T + pos), (LAS unsigned*)(blk + wid * 256), 4, 0, 0);
;         else __builtin_amdgcn_global_load_lds((const unsigned*)(rsc + (size_t)e * T + pos), (LAS unsigned*)(blk + 1024 + (wid - 4) * 256), 4, 0, 0);
.LBB0_1627:
	s_cmp_lg_u32 s22, s31
	s_cbranch_scc1 .LBB0_1636
	v_mbcnt_lo_u32_b32 v67, -1, 0
	v_mbcnt_hi_u32_b32 v67, -1, v67
	v_add_u32_e32 v65, s21, v204
	s_nop 0
	v_readfirstlane_b32 s76, v65
	v_add_u32_e32 v65, s49, v67
	s_mov_b32 m0, s76
	s_cmp_lt_i32 s85, 1
	v_add_u32_e32 v64, -1, v230
	v_min_i32_e32 v64, v65, v64
	v_ashrrev_i32_e32 v65, 31, v64
	v_lshlrev_b64 v[64:65], 2, v[64:65]
	v_lshl_add_u64 v[68:69], s[66:67], 0, v[64:65]
	v_lshl_add_u64 v[64:65], s[68:69], 0, v[64:65]
	v_cndmask_b32_e64 v65, v69, v65, s[4:5]
	v_cndmask_b32_e64 v64, v68, v64, s[4:5]
	global_load_lds_dword v[64:65], off
	s_cbranch_scc1 .LBB0_1633
	s_mov_b64 s[78:79], 0
	s_cmp_eq_u32 s85, 1
	s_mov_b64 s[76:77], 0
	s_cbranch_scc0 .LBB0_1631
	v_lshlrev_b32_e32 v64, 4, v67
	v_and_b32_e32 v64, 0x1f0, v64
	v_mov_b32_e32 v65, v193
	v_lshlrev_b32_e32 v66, 6, v67
	v_lshl_add_u64 v[64:65], s[70:71], 0, v[64:65]
	v_and_b32_e32 v66, 0xfffff800, v66
	s_mov_b64 s[76:77], -1
	s_movk_i32 s80, 0xc00
	s_and_b64 vcc, exec, s[78:79]
	s_cbranch_vccz .LBB0_1634
	s_branch .LBB0_1632
